# first MoE combine token loop rewritten: two tokens in flight (routing record two ahead, rows one ahead), 16-byte row loads/stores, packed fp8 unpack, DPP wave sum; on top of the attention rewrite
# speedup vs baseline: 1.0192x; 1.0192x over previous
.LBB0_1217:
	s_or_b64 exec, exec, s[24:25]
	s_cmpk_gt_i32 s94, 0x7fff
	s_waitcnt lgkmcnt(0)
	s_barrier
	s_cbranch_scc1 .LBB0_1222
	s_load_dwordx2 s[2:3], s[0:1], 0xc8
	v_lshlrev_b32_e32 v1, 4, v242
	v_lshlrev_b32_e32 v2, 3, v242
	v_mov_b32_e32 v3, 0
	v_mov_b32_e32 v124, 0x20000
	v_mov_b32_e32 v125, 0x80000
	v_mov_b32_e32 v126, 0xa0000
	v_mov_b32_e32 v127, 0x24d00
	s_waitcnt lgkmcnt(0)
	s_add_u32 s4, s2, 0x19000000
	s_addc_u32 s5, s3, 0
	s_add_u32 s6, s2, 0x2e800000
	s_addc_u32 s7, s3, 0
	s_add_u32 s8, s2, 0x3600000
	s_addc_u32 s9, s3, 0
	s_add_u32 s10, s2, 0x10000000
	s_addc_u32 s11, s3, 0
	s_add_u32 s12, s2, 0x36e0000
	s_addc_u32 s13, s3, 0
	s_mov_b32 s14, s94
	s_lshl_b32 s17, s14, 2
	s_add_u32 s30, s8, s17
	s_addc_u32 s31, s9, 0
	global_load_dword v4, v3, s[30:31]
	global_load_dword v5, v124, s[30:31]
	global_load_dword v6, v125, s[30:31]
	global_load_dword v7, v126, s[30:31]
	s_waitcnt vmcnt(0)
	v_lshrrev_b32_e32 v108, 24, v4
	v_lshrrev_b32_e32 v109, 24, v5
	v_lshl_add_u32 v108, v108, 2, v127
	v_lshl_add_u32 v109, v109, 2, v127
	ds_read_b32 v108, v108
	ds_read_b32 v109, v109
	v_and_b32_e32 v110, 0xffffff, v4
	v_and_b32_e32 v111, 0xffffff, v5
	v_mul_f32_e32 v128, 0x3d000000, v6
	v_mul_f32_e32 v130, 0x3d000000, v7
	v_mov_b32_e32 v129, v128
	v_mov_b32_e32 v131, v130
	s_lshr_b32 s18, s14, 20
	s_lshl_b32 s17, s14, 12
	s_add_u32 s24, s4, s17
	s_addc_u32 s25, s5, s18
	global_load_dwordx4 v[12:15], v1, s[24:25] offset:0
	global_load_dwordx4 v[16:19], v1, s[24:25] offset:1024
	global_load_dwordx4 v[20:23], v1, s[24:25] offset:2048
	global_load_dwordx4 v[24:27], v1, s[24:25] offset:3072
	s_waitcnt lgkmcnt(0)
	v_add_u32_e32 v108, v108, v110
	v_add_u32_e32 v109, v109, v111
	s_nop 0
	v_readfirstlane_b32 s17, v108
	v_readfirstlane_b32 s18, v109
	s_nop 3
	s_lshr_b32 s31, s17, 21
	s_lshl_b32 s30, s17, 11
	s_add_u32 s26, s6, s30
	s_addc_u32 s27, s7, s31
	s_lshr_b32 s31, s18, 21
	s_lshl_b32 s30, s18, 11
	s_add_u32 s28, s6, s30
	s_addc_u32 s29, s7, s31
	global_load_dwordx2 v[28:29], v2, s[26:27] offset:0
	global_load_dwordx2 v[30:31], v2, s[26:27] offset:512
	global_load_dwordx2 v[32:33], v2, s[26:27] offset:1024
	global_load_dwordx2 v[34:35], v2, s[26:27] offset:1536
	global_load_dwordx2 v[36:37], v2, s[28:29] offset:0
	global_load_dwordx2 v[38:39], v2, s[28:29] offset:512
	global_load_dwordx2 v[40:41], v2, s[28:29] offset:1024
	global_load_dwordx2 v[42:43], v2, s[28:29] offset:1536
	s_add_i32 s15, s14, s92
	s_cmpk_lt_u32 s15, 0x8000
	s_cselect_b32 s15, s15, s14
	s_lshl_b32 s17, s15, 2
	s_add_u32 s30, s8, s17
	s_addc_u32 s31, s9, 0
	global_load_dword v8, v3, s[30:31]
	global_load_dword v9, v124, s[30:31]
	global_load_dword v10, v125, s[30:31]
	global_load_dword v11, v126, s[30:31]
	s_waitcnt vmcnt(0)
.Lcb_loop:
	s_waitcnt vmcnt(5)
	v_lshrrev_b32_e32 v108, 24, v8
	v_lshrrev_b32_e32 v109, 24, v9
	v_lshl_add_u32 v108, v108, 2, v127
	v_lshl_add_u32 v109, v109, 2, v127
	ds_read_b32 v108, v108
	ds_read_b32 v109, v109
	v_and_b32_e32 v110, 0xffffff, v8
	v_and_b32_e32 v111, 0xffffff, v9
	v_mul_f32_e32 v132, 0x3d000000, v10
	v_mul_f32_e32 v134, 0x3d000000, v11
	v_mov_b32_e32 v133, v132
	v_mov_b32_e32 v135, v134
	s_lshr_b32 s18, s15, 20
	s_lshl_b32 s17, s15, 12
	s_add_u32 s24, s4, s17
	s_addc_u32 s25, s5, s18
	global_load_dwordx4 v[44:47], v1, s[24:25] offset:0
	global_load_dwordx4 v[48:51], v1, s[24:25] offset:1024
	global_load_dwordx4 v[52:55], v1, s[24:25] offset:2048
	global_load_dwordx4 v[56:59], v1, s[24:25] offset:3072
	s_waitcnt lgkmcnt(0)
	v_add_u32_e32 v108, v108, v110
	v_add_u32_e32 v109, v109, v111
	s_nop 0
	v_readfirstlane_b32 s17, v108
	v_readfirstlane_b32 s18, v109
	s_nop 3
	s_lshr_b32 s31, s17, 21
	s_lshl_b32 s30, s17, 11
	s_add_u32 s26, s6, s30
	s_addc_u32 s27, s7, s31
	s_lshr_b32 s31, s18, 21
	s_lshl_b32 s30, s18, 11
	s_add_u32 s28, s6, s30
	s_addc_u32 s29, s7, s31
	global_load_dwordx2 v[60:61], v2, s[26:27] offset:0
	global_load_dwordx2 v[62:63], v2, s[26:27] offset:512
	global_load_dwordx2 v[64:65], v2, s[26:27] offset:1024
	global_load_dwordx2 v[66:67], v2, s[26:27] offset:1536
	global_load_dwordx2 v[68:69], v2, s[28:29] offset:0
	global_load_dwordx2 v[70:71], v2, s[28:29] offset:512
	global_load_dwordx2 v[72:73], v2, s[28:29] offset:1024
	global_load_dwordx2 v[74:75], v2, s[28:29] offset:1536
	s_add_i32 s16, s15, s92
	s_cmpk_lt_u32 s16, 0x8000
	s_cselect_b32 s16, s16, s15
	s_lshl_b32 s17, s16, 2
	s_add_u32 s30, s8, s17
	s_addc_u32 s31, s9, 0
	global_load_dword v4, v3, s[30:31]
	global_load_dword v5, v124, s[30:31]
	global_load_dword v6, v125, s[30:31]
	global_load_dword v7, v126, s[30:31]
	s_lshr_b32 s18, s14, 20
	s_lshl_b32 s17, s14, 12
	s_add_u32 s34, s10, s17
	s_addc_u32 s35, s11, s18
	s_lshl_b32 s17, s14, 2
	s_add_u32 s36, s12, s17
	s_addc_u32 s37, s13, 0
	s_waitcnt vmcnt(25)
	v_lshlrev_b32_e32 v76, 16, v12
	v_and_b32_e32 v77, 0xffff0000, v12
	v_lshlrev_b32_e32 v78, 16, v13
	v_and_b32_e32 v79, 0xffff0000, v13
	v_lshlrev_b32_e32 v80, 16, v14
	v_and_b32_e32 v81, 0xffff0000, v14
	v_lshlrev_b32_e32 v82, 16, v15
	v_and_b32_e32 v83, 0xffff0000, v15
	v_lshlrev_b32_e32 v84, 16, v16
	v_and_b32_e32 v85, 0xffff0000, v16
	v_lshlrev_b32_e32 v86, 16, v17
	v_and_b32_e32 v87, 0xffff0000, v17
	v_lshlrev_b32_e32 v88, 16, v18
	v_and_b32_e32 v89, 0xffff0000, v18
	v_lshlrev_b32_e32 v90, 16, v19
	v_and_b32_e32 v91, 0xffff0000, v19
	v_lshlrev_b32_e32 v92, 16, v20
	v_and_b32_e32 v93, 0xffff0000, v20
	v_lshlrev_b32_e32 v94, 16, v21
	v_and_b32_e32 v95, 0xffff0000, v21
	v_lshlrev_b32_e32 v96, 16, v22
	v_and_b32_e32 v97, 0xffff0000, v22
	v_lshlrev_b32_e32 v98, 16, v23
	v_and_b32_e32 v99, 0xffff0000, v23
	v_lshlrev_b32_e32 v100, 16, v24
	v_and_b32_e32 v101, 0xffff0000, v24
	v_lshlrev_b32_e32 v102, 16, v25
	v_and_b32_e32 v103, 0xffff0000, v25
	v_lshlrev_b32_e32 v104, 16, v26
	v_and_b32_e32 v105, 0xffff0000, v26
	v_lshlrev_b32_e32 v106, 16, v27
	v_and_b32_e32 v107, 0xffff0000, v27
	v_cvt_pk_f32_fp8_e32 v[108:109], v28
	v_cvt_pk_f32_fp8_sdwa v[110:111], v28 src0_sel:WORD_1
	v_pk_fma_f32 v[76:77], v[108:109], v[128:129], v[76:77]
	v_pk_fma_f32 v[78:79], v[110:111], v[128:129], v[78:79]
	v_cvt_pk_f32_fp8_e32 v[108:109], v29
	v_cvt_pk_f32_fp8_sdwa v[110:111], v29 src0_sel:WORD_1
	v_pk_fma_f32 v[80:81], v[108:109], v[128:129], v[80:81]
	v_pk_fma_f32 v[82:83], v[110:111], v[128:129], v[82:83]
	v_cvt_pk_f32_fp8_e32 v[108:109], v30
	v_cvt_pk_f32_fp8_sdwa v[110:111], v30 src0_sel:WORD_1
	v_pk_fma_f32 v[84:85], v[108:109], v[128:129], v[84:85]
	v_pk_fma_f32 v[86:87], v[110:111], v[128:129], v[86:87]
	v_cvt_pk_f32_fp8_e32 v[108:109], v31
	v_cvt_pk_f32_fp8_sdwa v[110:111], v31 src0_sel:WORD_1
	v_pk_fma_f32 v[88:89], v[108:109], v[128:129], v[88:89]
	v_pk_fma_f32 v[90:91], v[110:111], v[128:129], v[90:91]
	v_cvt_pk_f32_fp8_e32 v[108:109], v32
	v_cvt_pk_f32_fp8_sdwa v[110:111], v32 src0_sel:WORD_1
	v_pk_fma_f32 v[92:93], v[108:109], v[128:129], v[92:93]
	v_pk_fma_f32 v[94:95], v[110:111], v[128:129], v[94:95]
	v_cvt_pk_f32_fp8_e32 v[108:109], v33
	v_cvt_pk_f32_fp8_sdwa v[110:111], v33 src0_sel:WORD_1
	v_pk_fma_f32 v[96:97], v[108:109], v[128:129], v[96:97]
	v_pk_fma_f32 v[98:99], v[110:111], v[128:129], v[98:99]
	v_cvt_pk_f32_fp8_e32 v[108:109], v34
	v_cvt_pk_f32_fp8_sdwa v[110:111], v34 src0_sel:WORD_1
	v_pk_fma_f32 v[100:101], v[108:109], v[128:129], v[100:101]
	v_pk_fma_f32 v[102:103], v[110:111], v[128:129], v[102:103]
	v_cvt_pk_f32_fp8_e32 v[108:109], v35
	v_cvt_pk_f32_fp8_sdwa v[110:111], v35 src0_sel:WORD_1
	v_pk_fma_f32 v[104:105], v[108:109], v[128:129], v[104:105]
	v_pk_fma_f32 v[106:107], v[110:111], v[128:129], v[106:107]
	v_cvt_pk_f32_fp8_e32 v[108:109], v36
	v_cvt_pk_f32_fp8_sdwa v[110:111], v36 src0_sel:WORD_1
	v_pk_fma_f32 v[76:77], v[108:109], v[130:131], v[76:77]
	v_pk_fma_f32 v[78:79], v[110:111], v[130:131], v[78:79]
	v_cvt_pk_f32_fp8_e32 v[108:109], v37
	v_cvt_pk_f32_fp8_sdwa v[110:111], v37 src0_sel:WORD_1
	v_pk_fma_f32 v[80:81], v[108:109], v[130:131], v[80:81]
	v_pk_fma_f32 v[82:83], v[110:111], v[130:131], v[82:83]
	v_cvt_pk_f32_fp8_e32 v[108:109], v38
	v_cvt_pk_f32_fp8_sdwa v[110:111], v38 src0_sel:WORD_1
	v_pk_fma_f32 v[84:85], v[108:109], v[130:131], v[84:85]
	v_pk_fma_f32 v[86:87], v[110:111], v[130:131], v[86:87]
	v_cvt_pk_f32_fp8_e32 v[108:109], v39
	v_cvt_pk_f32_fp8_sdwa v[110:111], v39 src0_sel:WORD_1
	v_pk_fma_f32 v[88:89], v[108:109], v[130:131], v[88:89]
	v_pk_fma_f32 v[90:91], v[110:111], v[130:131], v[90:91]
	v_cvt_pk_f32_fp8_e32 v[108:109], v40
	v_cvt_pk_f32_fp8_sdwa v[110:111], v40 src0_sel:WORD_1
	v_pk_fma_f32 v[92:93], v[108:109], v[130:131], v[92:93]
	v_pk_fma_f32 v[94:95], v[110:111], v[130:131], v[94:95]
	v_cvt_pk_f32_fp8_e32 v[108:109], v41
	v_cvt_pk_f32_fp8_sdwa v[110:111], v41 src0_sel:WORD_1
	v_pk_fma_f32 v[96:97], v[108:109], v[130:131], v[96:97]
	v_pk_fma_f32 v[98:99], v[110:111], v[130:131], v[98:99]
	v_cvt_pk_f32_fp8_e32 v[108:109], v42
	v_cvt_pk_f32_fp8_sdwa v[110:111], v42 src0_sel:WORD_1
	v_pk_fma_f32 v[100:101], v[108:109], v[130:131], v[100:101]
	v_pk_fma_f32 v[102:103], v[110:111], v[130:131], v[102:103]
	v_cvt_pk_f32_fp8_e32 v[108:109], v43
	v_cvt_pk_f32_fp8_sdwa v[110:111], v43 src0_sel:WORD_1
	v_pk_fma_f32 v[104:105], v[108:109], v[130:131], v[104:105]
	v_pk_fma_f32 v[106:107], v[110:111], v[130:131], v[106:107]
	v_pk_mul_f32 v[108:109], v[76:77], v[76:77]
	v_pk_mul_f32 v[110:111], v[78:79], v[78:79]
	v_pk_fma_f32 v[108:109], v[80:81], v[80:81], v[108:109]
	v_pk_fma_f32 v[110:111], v[82:83], v[82:83], v[110:111]
	v_pk_fma_f32 v[108:109], v[84:85], v[84:85], v[108:109]
	v_pk_fma_f32 v[110:111], v[86:87], v[86:87], v[110:111]
	v_pk_fma_f32 v[108:109], v[88:89], v[88:89], v[108:109]
	v_pk_fma_f32 v[110:111], v[90:91], v[90:91], v[110:111]
	v_pk_fma_f32 v[108:109], v[92:93], v[92:93], v[108:109]
	v_pk_fma_f32 v[110:111], v[94:95], v[94:95], v[110:111]
	v_pk_fma_f32 v[108:109], v[96:97], v[96:97], v[108:109]
	v_pk_fma_f32 v[110:111], v[98:99], v[98:99], v[110:111]
	v_pk_fma_f32 v[108:109], v[100:101], v[100:101], v[108:109]
	v_pk_fma_f32 v[110:111], v[102:103], v[102:103], v[110:111]
	v_pk_fma_f32 v[108:109], v[104:105], v[104:105], v[108:109]
	v_pk_fma_f32 v[110:111], v[106:107], v[106:107], v[110:111]
	v_pk_add_f32 v[108:109], v[108:109], v[110:111]
	s_nop 0
	v_add_f32_e32 v108, v108, v109
	s_nop 1
	v_add_f32_dpp v108, v108, v108 quad_perm:[1,0,3,2] row_mask:0xf bank_mask:0xf
	s_nop 1
	v_add_f32_dpp v108, v108, v108 quad_perm:[2,3,0,1] row_mask:0xf bank_mask:0xf
	s_nop 1
	v_add_f32_dpp v108, v108, v108 row_ror:4 row_mask:0xf bank_mask:0xf
	s_nop 1
	v_add_f32_dpp v108, v108, v108 row_ror:8 row_mask:0xf bank_mask:0xf
	s_nop 1
	v_add_f32_dpp v108, v108, v108 row_bcast:15 row_mask:0xa bank_mask:0xf
	s_nop 1
	v_add_f32_dpp v108, v108, v108 row_bcast:31 row_mask:0xc bank_mask:0xf
	s_nop 1
	v_readlane_b32 s17, v108, 63
	s_nop 3
	v_mov_b32_e32 v108, s17
	v_mul_f32_e32 v108, 0x3a000000, v108
	v_add_f32_e32 v108, 0x358637bd, v108
	v_rsq_f32_e32 v112, v108
	s_nop 0
	v_mov_b32_e32 v113, v112
	v_mul_f32_e32 v114, v108, v112
	v_pk_mul_f32 v[76:77], v[76:77], v[112:113]
	v_pk_mul_f32 v[78:79], v[78:79], v[112:113]
	v_pk_mul_f32 v[80:81], v[80:81], v[112:113]
	v_pk_mul_f32 v[82:83], v[82:83], v[112:113]
	v_pk_mul_f32 v[84:85], v[84:85], v[112:113]
	v_pk_mul_f32 v[86:87], v[86:87], v[112:113]
	v_pk_mul_f32 v[88:89], v[88:89], v[112:113]
	v_pk_mul_f32 v[90:91], v[90:91], v[112:113]
	v_pk_mul_f32 v[92:93], v[92:93], v[112:113]
	v_pk_mul_f32 v[94:95], v[94:95], v[112:113]
	v_pk_mul_f32 v[96:97], v[96:97], v[112:113]
	v_pk_mul_f32 v[98:99], v[98:99], v[112:113]
	v_pk_mul_f32 v[100:101], v[100:101], v[112:113]
	v_pk_mul_f32 v[102:103], v[102:103], v[112:113]
	v_pk_mul_f32 v[104:105], v[104:105], v[112:113]
	v_pk_mul_f32 v[106:107], v[106:107], v[112:113]
	v_cvt_pk_bf16_f32 v76, v76, v77
	v_cvt_pk_bf16_f32 v77, v78, v79
	v_cvt_pk_bf16_f32 v78, v80, v81
	v_cvt_pk_bf16_f32 v79, v82, v83
	v_cvt_pk_bf16_f32 v80, v84, v85
	v_cvt_pk_bf16_f32 v81, v86, v87
	v_cvt_pk_bf16_f32 v82, v88, v89
	v_cvt_pk_bf16_f32 v83, v90, v91
	v_cvt_pk_bf16_f32 v84, v92, v93
	v_cvt_pk_bf16_f32 v85, v94, v95
	v_cvt_pk_bf16_f32 v86, v96, v97
	v_cvt_pk_bf16_f32 v87, v98, v99
	v_cvt_pk_bf16_f32 v88, v100, v101
	v_cvt_pk_bf16_f32 v89, v102, v103
	v_cvt_pk_bf16_f32 v90, v104, v105
	v_cvt_pk_bf16_f32 v91, v106, v107
	global_store_dwordx4 v1, v[76:79], s[34:35] offset:0
	global_store_dwordx4 v1, v[80:83], s[34:35] offset:1024
	global_store_dwordx4 v1, v[84:87], s[34:35] offset:2048
	global_store_dwordx4 v1, v[88:91], s[34:35] offset:3072
	global_store_dword v3, v114, s[36:37]
	s_add_i32 s14, s14, s92
	s_mov_b32 s15, s16
	s_cmpk_lt_u32 s14, 0x8000
	s_cbranch_scc0 .Lcb_done
	s_waitcnt vmcnt(5)
	v_lshrrev_b32_e32 v108, 24, v4
	v_lshrrev_b32_e32 v109, 24, v5
	v_lshl_add_u32 v108, v108, 2, v127
	v_lshl_add_u32 v109, v109, 2, v127
	ds_read_b32 v108, v108
	ds_read_b32 v109, v109
	v_and_b32_e32 v110, 0xffffff, v4
	v_and_b32_e32 v111, 0xffffff, v5
	v_mul_f32_e32 v128, 0x3d000000, v6
	v_mul_f32_e32 v130, 0x3d000000, v7
	v_mov_b32_e32 v129, v128
	v_mov_b32_e32 v131, v130
	s_lshr_b32 s18, s15, 20
	s_lshl_b32 s17, s15, 12
	s_add_u32 s24, s4, s17
	s_addc_u32 s25, s5, s18
	global_load_dwordx4 v[12:15], v1, s[24:25] offset:0
	global_load_dwordx4 v[16:19], v1, s[24:25] offset:1024
	global_load_dwordx4 v[20:23], v1, s[24:25] offset:2048
	global_load_dwordx4 v[24:27], v1, s[24:25] offset:3072
	s_waitcnt lgkmcnt(0)
	v_add_u32_e32 v108, v108, v110
	v_add_u32_e32 v109, v109, v111
	s_nop 0
	v_readfirstlane_b32 s17, v108
	v_readfirstlane_b32 s18, v109
	s_nop 3
	s_lshr_b32 s31, s17, 21
	s_lshl_b32 s30, s17, 11
	s_add_u32 s26, s6, s30
	s_addc_u32 s27, s7, s31
	s_lshr_b32 s31, s18, 21
	s_lshl_b32 s30, s18, 11
	s_add_u32 s28, s6, s30
	s_addc_u32 s29, s7, s31
	global_load_dwordx2 v[28:29], v2, s[26:27] offset:0
	global_load_dwordx2 v[30:31], v2, s[26:27] offset:512
	global_load_dwordx2 v[32:33], v2, s[26:27] offset:1024
	global_load_dwordx2 v[34:35], v2, s[26:27] offset:1536
	global_load_dwordx2 v[36:37], v2, s[28:29] offset:0
	global_load_dwordx2 v[38:39], v2, s[28:29] offset:512
	global_load_dwordx2 v[40:41], v2, s[28:29] offset:1024
	global_load_dwordx2 v[42:43], v2, s[28:29] offset:1536
	s_add_i32 s16, s15, s92
	s_cmpk_lt_u32 s16, 0x8000
	s_cselect_b32 s16, s16, s15
	s_lshl_b32 s17, s16, 2
	s_add_u32 s30, s8, s17
	s_addc_u32 s31, s9, 0
	global_load_dword v8, v3, s[30:31]
	global_load_dword v9, v124, s[30:31]
	global_load_dword v10, v125, s[30:31]
	global_load_dword v11, v126, s[30:31]
	s_lshr_b32 s18, s14, 20
	s_lshl_b32 s17, s14, 12
	s_add_u32 s34, s10, s17
	s_addc_u32 s35, s11, s18
	s_lshl_b32 s17, s14, 2
	s_add_u32 s36, s12, s17
	s_addc_u32 s37, s13, 0
	s_waitcnt vmcnt(25)
	v_lshlrev_b32_e32 v76, 16, v44
	v_and_b32_e32 v77, 0xffff0000, v44
	v_lshlrev_b32_e32 v78, 16, v45
	v_and_b32_e32 v79, 0xffff0000, v45
	v_lshlrev_b32_e32 v80, 16, v46
	v_and_b32_e32 v81, 0xffff0000, v46
	v_lshlrev_b32_e32 v82, 16, v47
	v_and_b32_e32 v83, 0xffff0000, v47
	v_lshlrev_b32_e32 v84, 16, v48
	v_and_b32_e32 v85, 0xffff0000, v48
	v_lshlrev_b32_e32 v86, 16, v49
	v_and_b32_e32 v87, 0xffff0000, v49
	v_lshlrev_b32_e32 v88, 16, v50
	v_and_b32_e32 v89, 0xffff0000, v50
	v_lshlrev_b32_e32 v90, 16, v51
	v_and_b32_e32 v91, 0xffff0000, v51
	v_lshlrev_b32_e32 v92, 16, v52
	v_and_b32_e32 v93, 0xffff0000, v52
	v_lshlrev_b32_e32 v94, 16, v53
	v_and_b32_e32 v95, 0xffff0000, v53
	v_lshlrev_b32_e32 v96, 16, v54
	v_and_b32_e32 v97, 0xffff0000, v54
	v_lshlrev_b32_e32 v98, 16, v55
	v_and_b32_e32 v99, 0xffff0000, v55
	v_lshlrev_b32_e32 v100, 16, v56
	v_and_b32_e32 v101, 0xffff0000, v56
	v_lshlrev_b32_e32 v102, 16, v57
	v_and_b32_e32 v103, 0xffff0000, v57
	v_lshlrev_b32_e32 v104, 16, v58
	v_and_b32_e32 v105, 0xffff0000, v58
	v_lshlrev_b32_e32 v106, 16, v59
	v_and_b32_e32 v107, 0xffff0000, v59
	v_cvt_pk_f32_fp8_e32 v[108:109], v60
	v_cvt_pk_f32_fp8_sdwa v[110:111], v60 src0_sel:WORD_1
	v_pk_fma_f32 v[76:77], v[108:109], v[132:133], v[76:77]
	v_pk_fma_f32 v[78:79], v[110:111], v[132:133], v[78:79]
	v_cvt_pk_f32_fp8_e32 v[108:109], v61
	v_cvt_pk_f32_fp8_sdwa v[110:111], v61 src0_sel:WORD_1
	v_pk_fma_f32 v[80:81], v[108:109], v[132:133], v[80:81]
	v_pk_fma_f32 v[82:83], v[110:111], v[132:133], v[82:83]
	v_cvt_pk_f32_fp8_e32 v[108:109], v62
	v_cvt_pk_f32_fp8_sdwa v[110:111], v62 src0_sel:WORD_1
	v_pk_fma_f32 v[84:85], v[108:109], v[132:133], v[84:85]
	v_pk_fma_f32 v[86:87], v[110:111], v[132:133], v[86:87]
	v_cvt_pk_f32_fp8_e32 v[108:109], v63
	v_cvt_pk_f32_fp8_sdwa v[110:111], v63 src0_sel:WORD_1
	v_pk_fma_f32 v[88:89], v[108:109], v[132:133], v[88:89]
	v_pk_fma_f32 v[90:91], v[110:111], v[132:133], v[90:91]
	v_cvt_pk_f32_fp8_e32 v[108:109], v64
	v_cvt_pk_f32_fp8_sdwa v[110:111], v64 src0_sel:WORD_1
	v_pk_fma_f32 v[92:93], v[108:109], v[132:133], v[92:93]
	v_pk_fma_f32 v[94:95], v[110:111], v[132:133], v[94:95]
	v_cvt_pk_f32_fp8_e32 v[108:109], v65
	v_cvt_pk_f32_fp8_sdwa v[110:111], v65 src0_sel:WORD_1
	v_pk_fma_f32 v[96:97], v[108:109], v[132:133], v[96:97]
	v_pk_fma_f32 v[98:99], v[110:111], v[132:133], v[98:99]
	v_cvt_pk_f32_fp8_e32 v[108:109], v66
	v_cvt_pk_f32_fp8_sdwa v[110:111], v66 src0_sel:WORD_1
	v_pk_fma_f32 v[100:101], v[108:109], v[132:133], v[100:101]
	v_pk_fma_f32 v[102:103], v[110:111], v[132:133], v[102:103]
	v_cvt_pk_f32_fp8_e32 v[108:109], v67
	v_cvt_pk_f32_fp8_sdwa v[110:111], v67 src0_sel:WORD_1
	v_pk_fma_f32 v[104:105], v[108:109], v[132:133], v[104:105]
	v_pk_fma_f32 v[106:107], v[110:111], v[132:133], v[106:107]
	v_cvt_pk_f32_fp8_e32 v[108:109], v68
	v_cvt_pk_f32_fp8_sdwa v[110:111], v68 src0_sel:WORD_1
	v_pk_fma_f32 v[76:77], v[108:109], v[134:135], v[76:77]
	v_pk_fma_f32 v[78:79], v[110:111], v[134:135], v[78:79]
	v_cvt_pk_f32_fp8_e32 v[108:109], v69
	v_cvt_pk_f32_fp8_sdwa v[110:111], v69 src0_sel:WORD_1
	v_pk_fma_f32 v[80:81], v[108:109], v[134:135], v[80:81]
	v_pk_fma_f32 v[82:83], v[110:111], v[134:135], v[82:83]
	v_cvt_pk_f32_fp8_e32 v[108:109], v70
	v_cvt_pk_f32_fp8_sdwa v[110:111], v70 src0_sel:WORD_1
	v_pk_fma_f32 v[84:85], v[108:109], v[134:135], v[84:85]
	v_pk_fma_f32 v[86:87], v[110:111], v[134:135], v[86:87]
	v_cvt_pk_f32_fp8_e32 v[108:109], v71
	v_cvt_pk_f32_fp8_sdwa v[110:111], v71 src0_sel:WORD_1
	v_pk_fma_f32 v[88:89], v[108:109], v[134:135], v[88:89]
	v_pk_fma_f32 v[90:91], v[110:111], v[134:135], v[90:91]
	v_cvt_pk_f32_fp8_e32 v[108:109], v72
	v_cvt_pk_f32_fp8_sdwa v[110:111], v72 src0_sel:WORD_1
	v_pk_fma_f32 v[92:93], v[108:109], v[134:135], v[92:93]
	v_pk_fma_f32 v[94:95], v[110:111], v[134:135], v[94:95]
	v_cvt_pk_f32_fp8_e32 v[108:109], v73
	v_cvt_pk_f32_fp8_sdwa v[110:111], v73 src0_sel:WORD_1
	v_pk_fma_f32 v[96:97], v[108:109], v[134:135], v[96:97]
	v_pk_fma_f32 v[98:99], v[110:111], v[134:135], v[98:99]
	v_cvt_pk_f32_fp8_e32 v[108:109], v74
	v_cvt_pk_f32_fp8_sdwa v[110:111], v74 src0_sel:WORD_1
	v_pk_fma_f32 v[100:101], v[108:109], v[134:135], v[100:101]
	v_pk_fma_f32 v[102:103], v[110:111], v[134:135], v[102:103]
	v_cvt_pk_f32_fp8_e32 v[108:109], v75
	v_cvt_pk_f32_fp8_sdwa v[110:111], v75 src0_sel:WORD_1
	v_pk_fma_f32 v[104:105], v[108:109], v[134:135], v[104:105]
	v_pk_fma_f32 v[106:107], v[110:111], v[134:135], v[106:107]
	v_pk_mul_f32 v[108:109], v[76:77], v[76:77]
	v_pk_mul_f32 v[110:111], v[78:79], v[78:79]
	v_pk_fma_f32 v[108:109], v[80:81], v[80:81], v[108:109]
	v_pk_fma_f32 v[110:111], v[82:83], v[82:83], v[110:111]
	v_pk_fma_f32 v[108:109], v[84:85], v[84:85], v[108:109]
	v_pk_fma_f32 v[110:111], v[86:87], v[86:87], v[110:111]
	v_pk_fma_f32 v[108:109], v[88:89], v[88:89], v[108:109]
	v_pk_fma_f32 v[110:111], v[90:91], v[90:91], v[110:111]
	v_pk_fma_f32 v[108:109], v[92:93], v[92:93], v[108:109]
	v_pk_fma_f32 v[110:111], v[94:95], v[94:95], v[110:111]
	v_pk_fma_f32 v[108:109], v[96:97], v[96:97], v[108:109]
	v_pk_fma_f32 v[110:111], v[98:99], v[98:99], v[110:111]
	v_pk_fma_f32 v[108:109], v[100:101], v[100:101], v[108:109]
	v_pk_fma_f32 v[110:111], v[102:103], v[102:103], v[110:111]
	v_pk_fma_f32 v[108:109], v[104:105], v[104:105], v[108:109]
	v_pk_fma_f32 v[110:111], v[106:107], v[106:107], v[110:111]
	v_pk_add_f32 v[108:109], v[108:109], v[110:111]
	s_nop 0
	v_add_f32_e32 v108, v108, v109
	s_nop 1
	v_add_f32_dpp v108, v108, v108 quad_perm:[1,0,3,2] row_mask:0xf bank_mask:0xf
	s_nop 1
	v_add_f32_dpp v108, v108, v108 quad_perm:[2,3,0,1] row_mask:0xf bank_mask:0xf
	s_nop 1
	v_add_f32_dpp v108, v108, v108 row_ror:4 row_mask:0xf bank_mask:0xf
	s_nop 1
	v_add_f32_dpp v108, v108, v108 row_ror:8 row_mask:0xf bank_mask:0xf
	s_nop 1
	v_add_f32_dpp v108, v108, v108 row_bcast:15 row_mask:0xa bank_mask:0xf
	s_nop 1
	v_add_f32_dpp v108, v108, v108 row_bcast:31 row_mask:0xc bank_mask:0xf
	s_nop 1
	v_readlane_b32 s17, v108, 63
	s_nop 3
	v_mov_b32_e32 v108, s17
	v_mul_f32_e32 v108, 0x3a000000, v108
	v_add_f32_e32 v108, 0x358637bd, v108
	v_rsq_f32_e32 v112, v108
	s_nop 0
	v_mov_b32_e32 v113, v112
	v_mul_f32_e32 v114, v108, v112
	v_pk_mul_f32 v[76:77], v[76:77], v[112:113]
	v_pk_mul_f32 v[78:79], v[78:79], v[112:113]
	v_pk_mul_f32 v[80:81], v[80:81], v[112:113]
	v_pk_mul_f32 v[82:83], v[82:83], v[112:113]
	v_pk_mul_f32 v[84:85], v[84:85], v[112:113]
	v_pk_mul_f32 v[86:87], v[86:87], v[112:113]
	v_pk_mul_f32 v[88:89], v[88:89], v[112:113]
	v_pk_mul_f32 v[90:91], v[90:91], v[112:113]
	v_pk_mul_f32 v[92:93], v[92:93], v[112:113]
	v_pk_mul_f32 v[94:95], v[94:95], v[112:113]
	v_pk_mul_f32 v[96:97], v[96:97], v[112:113]
	v_pk_mul_f32 v[98:99], v[98:99], v[112:113]
	v_pk_mul_f32 v[100:101], v[100:101], v[112:113]
	v_pk_mul_f32 v[102:103], v[102:103], v[112:113]
	v_pk_mul_f32 v[104:105], v[104:105], v[112:113]
	v_pk_mul_f32 v[106:107], v[106:107], v[112:113]
	v_cvt_pk_bf16_f32 v76, v76, v77
	v_cvt_pk_bf16_f32 v77, v78, v79
	v_cvt_pk_bf16_f32 v78, v80, v81
	v_cvt_pk_bf16_f32 v79, v82, v83
	v_cvt_pk_bf16_f32 v80, v84, v85
	v_cvt_pk_bf16_f32 v81, v86, v87
	v_cvt_pk_bf16_f32 v82, v88, v89
	v_cvt_pk_bf16_f32 v83, v90, v91
	v_cvt_pk_bf16_f32 v84, v92, v93
	v_cvt_pk_bf16_f32 v85, v94, v95
	v_cvt_pk_bf16_f32 v86, v96, v97
	v_cvt_pk_bf16_f32 v87, v98, v99
	v_cvt_pk_bf16_f32 v88, v100, v101
	v_cvt_pk_bf16_f32 v89, v102, v103
	v_cvt_pk_bf16_f32 v90, v104, v105
	v_cvt_pk_bf16_f32 v91, v106, v107
	global_store_dwordx4 v1, v[76:79], s[34:35] offset:0
	global_store_dwordx4 v1, v[80:83], s[34:35] offset:1024
	global_store_dwordx4 v1, v[84:87], s[34:35] offset:2048
	global_store_dwordx4 v1, v[88:91], s[34:35] offset:3072
	global_store_dword v3, v114, s[36:37]
	s_add_i32 s14, s14, s92
	s_mov_b32 s15, s16
	s_cmpk_lt_u32 s14, 0x8000
	s_cbranch_scc1 .Lcb_loop
.Lcb_done:
.LBB0_1222:
	s_cmp_gt_i32 s47, 13
	s_cselect_b64 s[6:7], -1, 0
	s_and_b64 s[2:3], s[20:21], s[6:7]
	s_andn2_b64 vcc, exec, s[2:3]
	s_cbranch_vccnz .LBB0_1276
	s_waitcnt vmcnt(0)
	s_waitcnt vmcnt(0) lgkmcnt(0)
	s_barrier
	s_mov_b64 s[8:9], exec
	v_readlane_b32 s2, v252, 5
	v_readlane_b32 s3, v252, 6
	s_and_b64 s[2:3], s[8:9], s[2:3]
	s_mov_b64 exec, s[2:3]
	s_cbranch_execz .LBB0_1275
	s_add_i32 s2, 0, 0x24c40
	v_mov_b32_e32 v1, s2
	s_waitcnt vmcnt(0) expcnt(0) lgkmcnt(0)
	ds_read_b32 v3, v1
	s_add_i32 s2, 0, 0x24c44
	v_mov_b32_e32 v1, s2
	ds_read_b32 v1, v1
	s_waitcnt lgkmcnt(1)
	v_cmp_ne_u32_e32 vcc, 0, v3
	s_cbranch_vccnz .LBB0_1239
	s_add_u32 s10, s44, 0x4200
	s_addc_u32 s11, s45, 0
	s_add_u32 s12, s44, 0x4400
	s_addc_u32 s13, s45, 0
	s_add_u32 s14, s44, 0x4500
	s_addc_u32 s15, s45, 0
	s_add_u32 s16, s44, 0x4600
	s_addc_u32 s17, s45, 0
	s_add_u32 s18, s44, 0x4700
	s_addc_u32 s19, s45, 0
	s_add_u32 s20, s44, 0x4800
	s_addc_u32 s21, s45, 0
	s_add_u32 s22, s44, 0x4900
	s_addc_u32 s23, s45, 0
	s_add_u32 s24, s44, 0x4a00
	s_addc_u32 s25, s45, 0
	s_add_u32 s26, s44, 0x4b00
	s_addc_u32 s27, s45, 0
	s_add_u32 s28, s44, 0x4c00
	s_addc_u32 s29, s45, 0
	s_add_u32 s30, s44, 0x4d00
	s_addc_u32 s31, s45, 0
	s_add_u32 s34, s44, 0x4e00
	s_addc_u32 s35, s45, 0
	s_add_u32 s36, s44, 0x4f00
	v_readlane_b32 s4, v252, 0
	s_addc_u32 s37, s45, 0
	v_readlane_b32 s5, v252, 1
	s_add_u32 s38, s44, 0x5000
	s_load_dwordx2 s[2:3], s[4:5], 0x4
	s_addc_u32 s39, s45, 0
	s_add_u32 s40, s44, 0x5100
	s_addc_u32 s41, s45, 0
	s_add_u32 s54, s44, 0x5200
	s_addc_u32 s55, s45, 0
	s_waitcnt lgkmcnt(0)
	s_mul_i32 s2, s2, s91
	s_add_u32 s56, s44, 0x5300
	s_mul_i32 s2, s2, s3
	s_addc_u32 s57, s45, 0
	s_mov_b32 s3, 1
	v_mov_b32_e32 v17, 0
	s_branch .LBB0_1227
